# speedup vs baseline: 1.0238x; 1.0020x over previous
_Z9ln_kernelILi2EEvPKiPKfS3_PfS3_S3_PDF16_:
	s_load_dwordx8 s[4:11], s[0:1], 0x8
	v_and_b32_e32 v12, 63, v0
	v_lshrrev_b32_e32 v0, 6, v0
	v_lshl_or_b32 v6, s2, 2, v0
	v_ashrrev_i32_e32 v7, 31, v6
	v_lshlrev_b64 v[2:3], 11, v[6:7]
	v_mov_b32_e32 v1, 0
	s_waitcnt lgkmcnt(0)
	v_lshl_add_u64 v[8:9], s[4:5], 0, v[2:3]
	v_lshlrev_b32_e32 v4, 3, v12
	v_mov_b32_e32 v5, v1
	v_lshl_add_u64 v[8:9], v[8:9], 0, v[4:5]
	s_mov_b64 s[2:3], 0x400000
	v_lshl_add_u64 v[10:11], v[8:9], 0, s[2:3]
	s_mov_b32 s2, 0x400000
	global_load_dwordx2 v[16:17], v[8:9], off
	global_load_dwordx2 v[18:19], v[8:9], off offset:512
	global_load_dwordx2 v[20:21], v[8:9], off offset:1024
	global_load_dwordx2 v[22:23], v[8:9], off offset:1536
	v_add_co_u32_e32 v8, vcc, s2, v8
	global_load_dwordx2 v[24:25], v[10:11], off offset:512
	global_load_dwordx2 v[26:27], v[10:11], off offset:1024
	global_load_dwordx2 v[28:29], v[10:11], off offset:1536
	v_addc_co_u32_e32 v9, vcc, 0, v9, vcc
	global_load_dwordx2 v[30:31], v[8:9], off
	v_lshlrev_b64 v[6:7], 12, v[6:7]
	v_lshlrev_b32_e32 v0, 4, v12
	v_lshl_add_u64 v[6:7], s[8:9], 0, v[6:7]
	v_lshl_add_u64 v[6:7], v[6:7], 0, v[0:1]
	global_load_dwordx4 v[8:11], v[6:7], off offset:1024
	global_load_dwordx4 v[12:15], v0, s[6:7] offset:1024
	global_load_dwordx4 v[64:67], v[6:7], off
	global_load_dwordx4 v[68:71], v[6:7], off offset:2048
	global_load_dwordx4 v[72:75], v[6:7], off offset:3072
	global_load_dwordx4 v[76:79], v0, s[6:7] offset:2048
	global_load_dwordx4 v[80:83], v0, s[6:7]
	global_load_dwordx4 v[84:87], v0, s[6:7] offset:3072
	s_waitcnt vmcnt(15)
	v_cvt_f32_f16_e32 v32, v16
	s_waitcnt vmcnt(14)
	v_cvt_f32_f16_e32 v36, v18
	v_cvt_f32_f16_sdwa v37, v18 dst_sel:DWORD dst_unused:UNUSED_PAD src0_sel:WORD_1
	v_cvt_f32_f16_e32 v38, v19
	v_cvt_f32_f16_sdwa v39, v19 dst_sel:DWORD dst_unused:UNUSED_PAD src0_sel:WORD_1
	s_waitcnt vmcnt(13)
	v_cvt_f32_f16_e32 v40, v20
	v_cvt_f32_f16_sdwa v41, v20 dst_sel:DWORD dst_unused:UNUSED_PAD src0_sel:WORD_1
	v_cvt_f32_f16_e32 v42, v21
	v_cvt_f32_f16_sdwa v43, v21 dst_sel:DWORD dst_unused:UNUSED_PAD src0_sel:WORD_1
	s_waitcnt vmcnt(12)
	v_cvt_f32_f16_e32 v44, v22
	v_cvt_f32_f16_sdwa v45, v22 dst_sel:DWORD dst_unused:UNUSED_PAD src0_sel:WORD_1
	v_cvt_f32_f16_e32 v46, v23
	v_cvt_f32_f16_sdwa v47, v23 dst_sel:DWORD dst_unused:UNUSED_PAD src0_sel:WORD_1
	s_waitcnt vmcnt(11)
	v_cvt_f32_f16_e32 v20, v24
	v_cvt_f32_f16_sdwa v21, v24 dst_sel:DWORD dst_unused:UNUSED_PAD src0_sel:WORD_1
	v_cvt_f32_f16_e32 v22, v25
	v_cvt_f32_f16_sdwa v23, v25 dst_sel:DWORD dst_unused:UNUSED_PAD src0_sel:WORD_1
	s_waitcnt vmcnt(10)
	v_cvt_f32_f16_e32 v24, v26
	v_cvt_f32_f16_sdwa v25, v26 dst_sel:DWORD dst_unused:UNUSED_PAD src0_sel:WORD_1
	v_cvt_f32_f16_e32 v26, v27
	v_cvt_f32_f16_sdwa v27, v27 dst_sel:DWORD dst_unused:UNUSED_PAD src0_sel:WORD_1
	s_waitcnt vmcnt(9)
	v_cvt_f32_f16_e32 v48, v28
	v_cvt_f32_f16_sdwa v49, v28 dst_sel:DWORD dst_unused:UNUSED_PAD src0_sel:WORD_1
	v_cvt_f32_f16_e32 v28, v29
	v_cvt_f32_f16_sdwa v29, v29 dst_sel:DWORD dst_unused:UNUSED_PAD src0_sel:WORD_1
	v_cvt_f32_f16_sdwa v33, v16 dst_sel:DWORD dst_unused:UNUSED_PAD src0_sel:WORD_1
	v_cvt_f32_f16_e32 v34, v17
	v_cvt_f32_f16_sdwa v35, v17 dst_sel:DWORD dst_unused:UNUSED_PAD src0_sel:WORD_1
	s_waitcnt vmcnt(8)
	v_cvt_f32_f16_e32 v50, v30
	v_cvt_f32_f16_sdwa v51, v30 dst_sel:DWORD dst_unused:UNUSED_PAD src0_sel:WORD_1
	v_cvt_f32_f16_e32 v52, v31
	v_cvt_f32_f16_sdwa v53, v31 dst_sel:DWORD dst_unused:UNUSED_PAD src0_sel:WORD_1
	s_waitcnt vmcnt(0)
	v_mov_b32_e32 v16, v64
	v_mov_b32_e32 v17, v65
	v_mov_b32_e32 v18, v66
	v_mov_b32_e32 v19, v67
	v_pk_add_f32 v[36:37], v[36:37], v[20:21]
	v_pk_add_f32 v[38:39], v[38:39], v[22:23]
	v_mov_b32_e32 v20, v68
	v_mov_b32_e32 v21, v69
	v_mov_b32_e32 v22, v70
	v_mov_b32_e32 v23, v71
	v_pk_add_f32 v[40:41], v[40:41], v[24:25]
	v_pk_add_f32 v[42:43], v[42:43], v[26:27]
	v_mov_b32_e32 v24, v72
	v_mov_b32_e32 v25, v73
	v_mov_b32_e32 v26, v74
	v_mov_b32_e32 v27, v75
	v_pk_add_f32 v[46:47], v[46:47], v[28:29]
	v_mov_b32_e32 v28, v76
	v_mov_b32_e32 v29, v77
	v_mov_b32_e32 v30, v78
	v_mov_b32_e32 v31, v79
	s_waitcnt vmcnt(5)
	v_pk_add_f32 v[36:37], v[8:9], v[36:37]
	v_pk_add_f32 v[38:39], v[10:11], v[38:39]
	v_mov_b32_e32 v8, v80
	v_mov_b32_e32 v9, v81
	v_mov_b32_e32 v10, v82
	v_mov_b32_e32 v11, v83
	v_pk_add_f32 v[44:45], v[44:45], v[48:49]
	v_pk_add_f32 v[48:49], v[32:33], v[50:51]
	v_pk_add_f32 v[50:51], v[34:35], v[52:53]
	v_mov_b32_e32 v32, v84
	v_mov_b32_e32 v33, v85
	v_mov_b32_e32 v34, v86
	v_mov_b32_e32 v35, v87
	s_waitcnt vmcnt(6)
	v_pk_add_f32 v[12:13], v[12:13], v[36:37]
	v_pk_add_f32 v[14:15], v[14:15], v[38:39]
	s_load_dwordx4 s[4:7], s[0:1], 0x28
	s_mov_b32 s0, 0xf800000
	s_waitcnt lgkmcnt(0)
	v_lshl_add_u64 v[2:3], s[6:7], 0, v[2:3]
	s_waitcnt vmcnt(4)
	v_pk_add_f32 v[20:21], v[20:21], v[40:41]
	v_pk_add_f32 v[22:23], v[22:23], v[42:43]
	v_pk_add_f32 v[40:41], v[16:17], v[48:49]
	v_pk_add_f32 v[42:43], v[18:19], v[50:51]
	s_waitcnt vmcnt(3)
	v_pk_add_f32 v[24:25], v[24:25], v[44:45]
	v_pk_add_f32 v[26:27], v[26:27], v[46:47]
	s_waitcnt vmcnt(2)
	v_pk_add_f32 v[16:17], v[28:29], v[20:21]
	v_pk_add_f32 v[18:19], v[30:31], v[22:23]
	s_waitcnt vmcnt(1)
	v_pk_add_f32 v[8:9], v[8:9], v[40:41]
	v_pk_add_f32 v[10:11], v[10:11], v[42:43]
	v_mov_b32_e32 v28, v13
	v_mov_b32_e32 v29, v15
	s_waitcnt vmcnt(0)
	v_pk_add_f32 v[20:21], v[32:33], v[24:25]
	v_pk_add_f32 v[22:23], v[34:35], v[26:27]
	v_mov_b32_e32 v24, v8
	v_mov_b32_e32 v25, v10
	v_mov_b32_e32 v26, v9
	v_mov_b32_e32 v27, v11
	v_pk_add_f32 v[24:25], v[24:25], v[26:27]
	v_mov_b32_e32 v26, v12
	v_mov_b32_e32 v27, v14
	v_pk_add_f32 v[26:27], v[26:27], v[28:29]
	v_add_f32_e32 v1, v24, v25
	v_pk_add_f32 v[26:27], v[26:27], v[26:27] op_sel:[0,1] op_sel_hi:[1,0]
	v_pk_add_f32 v[28:29], v[16:17], v[16:17] op_sel:[0,1] op_sel_hi:[1,0]
	v_pk_add_f32 v[30:31], v[18:19], v[18:19] op_sel:[0,1] op_sel_hi:[1,0]
	v_add_f32_e32 v24, 0, v1
	v_mov_b32_e32 v25, v20
	v_mov_b32_e32 v27, v21
	v_mov_b32_e32 v29, v22
	v_mov_b32_e32 v31, v23
	v_pk_add_f32 v[24:25], v[24:25], v[26:27]
	v_pk_add_f32 v[26:27], v[28:29], v[30:31]
	s_nop 0
	v_pk_add_f32 v[24:25], v[24:25], v[26:27]
	s_nop 0
	v_add_f32_e32 v1, v24, v25
	v_mbcnt_lo_u32_b32 v24, -1, 0
	v_mbcnt_hi_u32_b32 v24, -1, v24
	v_and_b32_e32 v25, 64, v24
	v_add_u32_e32 v25, 64, v25
	v_xor_b32_e32 v26, 32, v24
	v_cmp_lt_i32_e32 vcc, v26, v25
	s_nop 1
	v_cndmask_b32_e32 v26, v24, v26, vcc
	v_lshlrev_b32_e32 v52, 2, v26
	v_mov_b32_e32 v26, v1
	s_waitcnt lgkmcnt(0)
	s_nop 1
	v_permlane32_swap_b32_e32 v1, v26
	v_add_f32_e32 v1, v1, v26
	v_xor_b32_e32 v26, 16, v24
	v_cmp_lt_i32_e32 vcc, v26, v25
	s_nop 1
	v_cndmask_b32_e32 v26, v24, v26, vcc
	v_lshlrev_b32_e32 v53, 2, v26
	v_mov_b32_e32 v26, v1
	s_waitcnt lgkmcnt(0)
	s_nop 1
	v_permlane16_swap_b32_e32 v1, v26
	v_add_f32_e32 v1, v1, v26
	v_xor_b32_e32 v26, 8, v24
	v_cmp_lt_i32_e32 vcc, v26, v25
	s_nop 1
	v_cndmask_b32_e32 v26, v24, v26, vcc
	v_lshlrev_b32_e32 v54, 2, v26
	s_waitcnt lgkmcnt(0)
	s_nop 1
	v_add_f32_dpp v1, v1, v1 row_ror:8 row_mask:0xf bank_mask:0xf
	v_xor_b32_e32 v26, 4, v24
	v_cmp_lt_i32_e32 vcc, v26, v25
	s_nop 1
	v_cndmask_b32_e32 v26, v24, v26, vcc
	v_lshlrev_b32_e32 v55, 2, v26
	s_waitcnt lgkmcnt(0)
	s_nop 1
	v_add_f32_dpp v1, v1, v1 row_ror:4 row_mask:0xf bank_mask:0xf
	v_xor_b32_e32 v26, 2, v24
	v_cmp_lt_i32_e32 vcc, v26, v25
	s_nop 1
	v_cndmask_b32_e32 v26, v24, v26, vcc
	v_lshlrev_b32_e32 v56, 2, v26
	s_waitcnt lgkmcnt(0)
	s_nop 1
	v_add_f32_dpp v1, v1, v1 row_ror:2 row_mask:0xf bank_mask:0xf
	v_xor_b32_e32 v26, 1, v24
	v_cmp_lt_i32_e32 vcc, v26, v25
	s_nop 1
	v_cndmask_b32_e32 v24, v24, v26, vcc
	v_lshlrev_b32_e32 v57, 2, v24
	s_waitcnt lgkmcnt(0)
	s_nop 1
	v_add_f32_dpp v1, v1, v1 row_ror:1 row_mask:0xf bank_mask:0xf
	v_mul_f32_e32 v24, 0x3a800000, v1
	v_pk_add_f32 v[36:37], v[8:9], v[24:25] op_sel_hi:[1,0] neg_lo:[0,1] neg_hi:[0,1]
	v_pk_add_f32 v[38:39], v[10:11], v[24:25] op_sel_hi:[1,0] neg_lo:[0,1] neg_hi:[0,1]
	v_mov_b32_e32 v28, v37
	v_mov_b32_e32 v29, v39
	v_pk_add_f32 v[40:41], v[12:13], v[24:25] op_sel_hi:[1,0] neg_lo:[0,1] neg_hi:[0,1]
	v_pk_add_f32 v[42:43], v[14:15], v[24:25] op_sel_hi:[1,0] neg_lo:[0,1] neg_hi:[0,1]
	v_mov_b32_e32 v26, v36
	v_mov_b32_e32 v27, v38
	v_pk_mul_f32 v[28:29], v[28:29], v[28:29]
	v_mov_b32_e32 v30, v41
	v_mov_b32_e32 v31, v43
	v_pk_fma_f32 v[26:27], v[26:27], v[26:27], v[28:29]
	v_mov_b32_e32 v28, v40
	v_mov_b32_e32 v29, v42
	v_pk_mul_f32 v[30:31], v[30:31], v[30:31]
	v_pk_add_f32 v[44:45], v[16:17], v[24:25] op_sel_hi:[1,0] neg_lo:[0,1] neg_hi:[0,1]
	v_pk_fma_f32 v[28:29], v[28:29], v[28:29], v[30:31]
	v_mul_f32_e32 v30, v44, v44
	v_pk_fma_f32 v[30:31], v[44:45], v[44:45], v[30:31] op_sel_hi:[1,1,0]
	v_pk_add_f32 v[46:47], v[18:19], v[24:25] op_sel_hi:[1,0] neg_lo:[0,1] neg_hi:[0,1]
	v_pk_add_f32 v[48:49], v[20:21], v[24:25] op_sel_hi:[1,0] neg_lo:[0,1] neg_hi:[0,1]
	v_mul_f32_e32 v30, v46, v46
	v_pk_add_f32 v[50:51], v[22:23], v[24:25] op_sel_hi:[1,0] neg_lo:[0,1] neg_hi:[0,1]
	v_pk_fma_f32 v[32:33], v[46:47], v[46:47], v[30:31] op_sel_hi:[1,1,0]
	v_pk_mul_f32 v[34:35], v[48:49], v[48:49]
	v_pk_add_f32 v[26:27], v[26:27], v[26:27] op_sel_hi:[0,1]
	v_pk_add_f32 v[28:29], v[28:29], v[28:29] op_sel_hi:[0,1]
	v_pk_mul_f32 v[24:25], v[50:51], v[50:51]
	v_mov_b32_e32 v30, v34
	v_mov_b32_e32 v32, v35
	v_mov_b32_e32 v26, v24
	v_mov_b32_e32 v28, v25
	v_pk_add_f32 v[30:31], v[30:31], v[32:33]
	v_pk_add_f32 v[24:25], v[26:27], v[28:29]
	s_nop 0
	v_pk_add_f32 v[24:25], v[30:31], v[24:25]
	s_nop 0
	v_add_f32_e32 v1, v24, v25
	v_mov_b32_e32 v24, v1
	s_waitcnt lgkmcnt(0)
	s_nop 1
	v_permlane32_swap_b32_e32 v1, v24
	v_add_f32_e32 v1, v1, v24
	v_mov_b32_e32 v24, v1
	s_waitcnt lgkmcnt(0)
	s_nop 1
	v_permlane16_swap_b32_e32 v1, v24
	v_add_f32_e32 v1, v1, v24
	s_waitcnt lgkmcnt(0)
	s_nop 1
	v_add_f32_dpp v1, v1, v1 row_ror:8 row_mask:0xf bank_mask:0xf
	s_waitcnt lgkmcnt(0)
	s_nop 1
	v_add_f32_dpp v1, v1, v1 row_ror:4 row_mask:0xf bank_mask:0xf
	global_load_dwordx4 v[24:27], v0, s[10:11]
	global_load_dwordx4 v[28:31], v0, s[10:11] offset:1024
	s_waitcnt lgkmcnt(0)
	s_nop 1
	v_add_f32_dpp v1, v1, v1 row_ror:2 row_mask:0xf bank_mask:0xf
	global_store_dwordx4 v[6:7], v[8:11], off
	global_store_dwordx4 v[6:7], v[12:15], off offset:1024
	global_store_dwordx4 v[6:7], v[16:19], off offset:2048
	global_store_dwordx4 v[6:7], v[20:23], off offset:3072
	s_waitcnt lgkmcnt(0)
	s_nop 1
	v_add_f32_dpp v1, v1, v1 row_ror:1 row_mask:0xf bank_mask:0xf
	v_mov_b32_e32 v32, 0x3727c5ac
	v_fmac_f32_e32 v32, 0x3a800000, v1
	v_mul_f32_e32 v1, 0x4f800000, v32
	v_cmp_gt_f32_e32 vcc, s0, v32
	global_load_dwordx4 v[12:15], v0, s[4:5]
	global_load_dwordx4 v[16:19], v0, s[4:5] offset:1024
	v_cndmask_b32_e32 v1, v32, v1, vcc
	v_sqrt_f32_e32 v32, v1
	global_load_dwordx4 v[8:11], v0, s[10:11] offset:2048
	v_add_u32_e32 v6, -1, v32
	v_fma_f32 v7, -v6, v32, v1
	v_cmp_ge_f32_e64 s[0:1], 0, v7
	v_add_u32_e32 v7, 1, v32
	v_fma_f32 v20, -v7, v32, v1
	v_cndmask_b32_e64 v6, v32, v6, s[0:1]
	v_cmp_lt_f32_e64 s[0:1], 0, v20
	global_load_dwordx4 v[20:23], v0, s[4:5] offset:2048
	s_nop 0
	v_cndmask_b32_e64 v6, v6, v7, s[0:1]
	v_mul_f32_e32 v7, 0x37800000, v6
	v_cndmask_b32_e32 v6, v6, v7, vcc
	v_mov_b32_e32 v7, 0x260
	v_cmp_class_f32_e32 vcc, v1, v7
	s_nop 1
	v_cndmask_b32_e32 v1, v6, v1, vcc
	v_div_scale_f32 v32, s[0:1], v1, v1, 1.0
	v_rcp_f32_e32 v33, v32
	v_lshl_add_u64 v[6:7], v[2:3], 0, v[4:5]
	v_div_scale_f32 v34, vcc, 1.0, v1, 1.0
	v_fma_f32 v2, -v32, v33, 1.0
	v_fmac_f32_e32 v33, v2, v33
	v_mul_f32_e32 v35, v34, v33
	v_fma_f32 v2, -v32, v35, v34
	v_fmac_f32_e32 v35, v2, v33
	v_fma_f32 v32, -v32, v35, v34
	global_load_dwordx4 v[2:5], v0, s[10:11] offset:3072
	v_div_fmas_f32 v52, v32, v33, v35
	global_load_dwordx4 v[32:35], v0, s[4:5] offset:3072
	v_div_fixup_f32 v0, v52, v1, 1.0
	v_pk_mul_f32 v[36:37], v[36:37], v[0:1] op_sel_hi:[1,0]
	s_waitcnt vmcnt(5)
	v_pk_fma_f32 v[12:13], v[24:25], v[36:37], v[12:13]
	v_pk_mul_f32 v[24:25], v[38:39], v[0:1] op_sel_hi:[1,0]
	v_cvt_pk_f16_f32 v12, v12, v13
	v_pk_fma_f32 v[14:15], v[26:27], v[24:25], v[14:15]
	s_nop 0
	v_cvt_pk_f16_f32 v13, v14, v15
	global_store_dwordx2 v[6:7], v[12:13], off
	v_pk_mul_f32 v[12:13], v[40:41], v[0:1] op_sel_hi:[1,0]
	v_pk_mul_f32 v[14:15], v[42:43], v[0:1] op_sel_hi:[1,0]
	s_waitcnt vmcnt(5)
	v_pk_fma_f32 v[12:13], v[28:29], v[12:13], v[16:17]
	v_pk_fma_f32 v[14:15], v[30:31], v[14:15], v[18:19]
	v_cvt_pk_f16_f32 v12, v12, v13
	v_cvt_pk_f16_f32 v13, v14, v15
	global_store_dwordx2 v[6:7], v[12:13], off offset:512
	v_pk_mul_f32 v[12:13], v[44:45], v[0:1] op_sel_hi:[1,0]
	s_waitcnt vmcnt(4)
	v_pk_fma_f32 v[8:9], v[12:13], v[8:9], v[20:21]
	v_pk_mul_f32 v[12:13], v[46:47], v[0:1] op_sel_hi:[1,0]
	v_cvt_pk_f16_f32 v8, v8, v9
	v_pk_fma_f32 v[10:11], v[12:13], v[10:11], v[22:23]
	s_nop 0
	v_cvt_pk_f16_f32 v9, v10, v11
	global_store_dwordx2 v[6:7], v[8:9], off offset:1024
	v_pk_mul_f32 v[8:9], v[48:49], v[0:1] op_sel_hi:[1,0]
	v_pk_mul_f32 v[0:1], v[50:51], v[0:1] op_sel_hi:[1,0]
	s_waitcnt vmcnt(3)
	v_pk_fma_f32 v[2:3], v[8:9], v[2:3], v[32:33]
	v_pk_fma_f32 v[0:1], v[0:1], v[4:5], v[34:35]
	v_cvt_pk_f16_f32 v2, v2, v3
	v_cvt_pk_f16_f32 v3, v0, v1
	global_store_dwordx2 v[6:7], v[2:3], off offset:1536
	s_endpgm
	s_endpgm
	s_endpgm
	s_endpgm
	s_endpgm
	s_endpgm
	s_endpgm
	s_endpgm
	s_endpgm
	s_endpgm
	s_endpgm
	s_endpgm
	s_endpgm
	s_endpgm
	s_endpgm
	s_endpgm
	s_endpgm
	s_endpgm
	s_endpgm
	s_endpgm
	s_endpgm
	s_endpgm
	s_endpgm
	s_endpgm
	s_endpgm
	s_endpgm
	s_endpgm
	s_endpgm
	s_endpgm
	s_endpgm
	s_endpgm
	s_endpgm
	s_endpgm
	s_endpgm
	s_endpgm
	s_endpgm
	s_endpgm
	s_endpgm
	s_endpgm
	s_endpgm
	s_endpgm
	s_endpgm
	s_endpgm
	s_endpgm
	s_endpgm
	s_endpgm
	s_endpgm
	s_endpgm
	s_endpgm

	.amdhsa_kernel _Z9ln_kernelILi2EEvPKiPKfS3_PfS3_S3_PDF16_
		.amdhsa_group_segment_fixed_size 0
		.amdhsa_private_segment_fixed_size 0
		.amdhsa_kernarg_size 56
		.amdhsa_user_sgpr_count 2
		.amdhsa_user_sgpr_dispatch_ptr 0
		.amdhsa_user_sgpr_queue_ptr 0
		.amdhsa_user_sgpr_kernarg_segment_ptr 1
		.amdhsa_user_sgpr_dispatch_id 0
		.amdhsa_user_sgpr_kernarg_preload_length 0
		.amdhsa_user_sgpr_kernarg_preload_offset 0
		.amdhsa_user_sgpr_private_segment_size 0
		.amdhsa_uses_dynamic_stack 0
		.amdhsa_enable_private_segment 0
		.amdhsa_system_sgpr_workgroup_id_x 1
		.amdhsa_system_sgpr_workgroup_id_y 0
		.amdhsa_system_sgpr_workgroup_id_z 0
		.amdhsa_system_sgpr_workgroup_info 0
		.amdhsa_system_vgpr_workitem_id 0
		.amdhsa_next_free_vgpr 88
		.amdhsa_next_free_sgpr 12
		.amdhsa_accum_offset 88
		.amdhsa_reserve_vcc 1
		.amdhsa_float_round_mode_32 0
		.amdhsa_float_round_mode_16_64 0
		.amdhsa_float_denorm_mode_32 3
		.amdhsa_float_denorm_mode_16_64 3
		.amdhsa_dx10_clamp 1
		.amdhsa_ieee_mode 1
		.amdhsa_fp16_overflow 0
		.amdhsa_tg_split 0
		.amdhsa_exception_fp_ieee_invalid_op 0
		.amdhsa_exception_fp_denorm_src 0
		.amdhsa_exception_fp_ieee_div_zero 0
		.amdhsa_exception_fp_ieee_overflow 0
		.amdhsa_exception_fp_ieee_underflow 0
		.amdhsa_exception_fp_ieee_inexact 0
		.amdhsa_exception_int_div_zero 0
	.end_amdhsa_kernel

amdhsa.kernels:
  - .agpr_count:     0
    .args:
      - .offset:         0
        .size:           400
        .value_kind:     by_value
    .group_segment_fixed_size: 33280
    .kernarg_segment_align: 8
    .kernarg_segment_size: 400
    .language:       OpenCL C
    .language_version:
      - 2
      - 0
    .max_flat_workgroup_size: 256
    .name:           _Z10wt_convert7CvtJobs
    .private_segment_fixed_size: 0
    .sgpr_count:     54
    .sgpr_spill_count: 0
    .symbol:         _Z10wt_convert7CvtJobs.kd
    .uniform_work_group_size: 1
    .uses_dynamic_stack: false
    .vgpr_count:     45
    .vgpr_spill_count: 0
    .wavefront_size: 64
  - .agpr_count:     0
    .args:
      - .actual_access:  read_only
        .address_space:  global
        .offset:         0
        .size:           8
        .value_kind:     global_buffer
      - .actual_access:  read_only
        .address_space:  global
        .offset:         8
        .size:           8
        .value_kind:     global_buffer
      - .actual_access:  read_only
        .address_space:  global
        .offset:         16
        .size:           8
        .value_kind:     global_buffer
      - .actual_access:  write_only
        .address_space:  global
        .offset:         24
        .size:           8
        .value_kind:     global_buffer
      - .actual_access:  read_only
        .address_space:  global
        .offset:         32
        .size:           8
        .value_kind:     global_buffer
      - .actual_access:  read_only
        .address_space:  global
        .offset:         40
        .size:           8
        .value_kind:     global_buffer
      - .actual_access:  write_only
        .address_space:  global
        .offset:         48
        .size:           8
        .value_kind:     global_buffer
      - .offset:         56
        .size:           400
        .value_kind:     by_value
    .group_segment_fixed_size: 33280
    .kernarg_segment_align: 8
    .kernarg_segment_size: 456
    .language:       OpenCL C
    .language_version:
      - 2
      - 0
    .max_flat_workgroup_size: 256
    .name:           _Z13embed_ln_convPKiPKfS2_PfS2_S2_PDF16_7CvtJobs
    .private_segment_fixed_size: 0
    .sgpr_count:     36
    .sgpr_spill_count: 0
    .symbol:         _Z13embed_ln_convPKiPKfS2_PfS2_S2_PDF16_7CvtJobs.kd
    .uniform_work_group_size: 1
    .uses_dynamic_stack: false
    .vgpr_count:     79
    .vgpr_spill_count: 0
    .wavefront_size: 64
  - .agpr_count:     0
    .args:
      - .address_space:  global
        .offset:         0
        .size:           8
        .value_kind:     global_buffer
      - .address_space:  global
        .offset:         8
        .size:           8
        .value_kind:     global_buffer
      - .actual_access:  write_only
        .address_space:  global
        .offset:         16
        .size:           8
        .value_kind:     global_buffer
      - .actual_access:  read_only
        .address_space:  global
        .offset:         24
        .size:           8
        .value_kind:     global_buffer
      - .offset:         32
        .size:           4
        .value_kind:     by_value
      - .offset:         36
        .size:           4
        .value_kind:     by_value
      - .offset:         40
        .size:           4
        .value_kind:     by_value
    .group_segment_fixed_size: 0
    .kernarg_segment_align: 8
    .kernarg_segment_size: 44
    .language:       OpenCL C
    .language_version:
      - 2
      - 0
    .max_flat_workgroup_size: 512
    .name:           _Z17gemm_256sq_8phasePKDF16_S0_PfPKfiii
    .private_segment_fixed_size: 0
    .sgpr_count:     47
    .sgpr_spill_count: 0
    .symbol:         _Z17gemm_256sq_8phasePKDF16_S0_PfPKfiii.kd
    .uniform_work_group_size: 1
    .uses_dynamic_stack: false
    .vgpr_count:     244
    .vgpr_spill_count: 0
    .wavefront_size: 64
  - .agpr_count:     0
    .args:
      - .actual_access:  read_only
        .address_space:  global
        .offset:         0
        .size:           8
        .value_kind:     global_buffer
      - .actual_access:  read_only
        .address_space:  global
        .offset:         8
        .size:           8
        .value_kind:     global_buffer
      - .actual_access:  read_only
        .address_space:  global
        .offset:         16
        .size:           8
        .value_kind:     global_buffer
      - .actual_access:  write_only
        .address_space:  global
        .offset:         24
        .size:           8
        .value_kind:     global_buffer
      - .offset:         32
        .size:           400
        .value_kind:     by_value
    .group_segment_fixed_size: 33280
    .kernarg_segment_align: 8
    .kernarg_segment_size: 432
    .language:       OpenCL C
    .language_version:
      - 2
      - 0
    .max_flat_workgroup_size: 256
    .name:           _Z11attn_kernelPKDF16_S0_S0_PDF16_7CvtJobs
    .private_segment_fixed_size: 0
    .sgpr_count:     36
    .sgpr_spill_count: 0
    .symbol:         _Z11attn_kernelPKDF16_S0_S0_PDF16_7CvtJobs.kd
    .uniform_work_group_size: 1
    .uses_dynamic_stack: false
    .vgpr_count:     116
    .vgpr_spill_count: 0
    .wavefront_size: 64
  - .agpr_count:     0
    .args:
      - .address_space:  global
        .offset:         0
        .size:           8
        .value_kind:     global_buffer
      - .address_space:  global
        .offset:         8
        .size:           8
        .value_kind:     global_buffer
      - .offset:         16
        .size:           4
        .value_kind:     by_value
      - .offset:         20
        .size:           4
        .value_kind:     by_value
      - .offset:         24
        .size:           4
        .value_kind:     by_value
      - .actual_access:  write_only
        .address_space:  global
        .offset:         32
        .size:           8
        .value_kind:     global_buffer
      - .actual_access:  read_only
        .address_space:  global
        .offset:         40
        .size:           8
        .value_kind:     global_buffer
      - .actual_access:  read_only
        .address_space:  global
        .offset:         48
        .size:           8
        .value_kind:     global_buffer
      - .offset:         56
        .size:           4
        .value_kind:     hidden_block_count_x
      - .offset:         60
        .size:           4
        .value_kind:     hidden_block_count_y
      - .offset:         64
        .size:           4
        .value_kind:     hidden_block_count_z
      - .offset:         68
        .size:           2
        .value_kind:     hidden_group_size_x
      - .offset:         70
        .size:           2
        .value_kind:     hidden_group_size_y
      - .offset:         72
        .size:           2
        .value_kind:     hidden_group_size_z
      - .offset:         74
        .size:           2
        .value_kind:     hidden_remainder_x
      - .offset:         76
        .size:           2
        .value_kind:     hidden_remainder_y
      - .offset:         78
        .size:           2
        .value_kind:     hidden_remainder_z
      - .offset:         96
        .size:           8
        .value_kind:     hidden_global_offset_x
      - .offset:         104
        .size:           8
        .value_kind:     hidden_global_offset_y
      - .offset:         112
        .size:           8
        .value_kind:     hidden_global_offset_z
      - .offset:         120
        .size:           2
        .value_kind:     hidden_grid_dims
      - .offset:         176
        .size:           4
        .value_kind:     hidden_dynamic_lds_size
    .group_segment_fixed_size: 0
    .kernarg_segment_align: 8
    .kernarg_segment_size: 312
    .language:       OpenCL C
    .language_version:
      - 2
      - 0
    .max_flat_workgroup_size: 512
    .name:           _Z5gemm8ILi192ELi2ELi3ELi0ELi1ELi16EEvPKDF16_S1_iiiPDF16_PfPKf
    .private_segment_fixed_size: 0
    .sgpr_count:     34
    .sgpr_spill_count: 0
    .symbol:         _Z5gemm8ILi192ELi2ELi3ELi0ELi1ELi16EEvPKDF16_S1_iiiPDF16_PfPKf.kd
    .uniform_work_group_size: 1
    .uses_dynamic_stack: false
    .vgpr_count:     125
    .vgpr_spill_count: 0
    .wavefront_size: 64
  - .agpr_count:     0
    .args:
      - .address_space:  global
        .offset:         0
        .size:           8
        .value_kind:     global_buffer
      - .address_space:  global
        .offset:         8
        .size:           8
        .value_kind:     global_buffer
      - .offset:         16
        .size:           4
        .value_kind:     by_value
      - .offset:         20
        .size:           4
        .value_kind:     by_value
      - .offset:         24
        .size:           4
        .value_kind:     by_value
      - .actual_access:  write_only
        .address_space:  global
        .offset:         32
        .size:           8
        .value_kind:     global_buffer
      - .actual_access:  read_only
        .address_space:  global
        .offset:         40
        .size:           8
        .value_kind:     global_buffer
      - .actual_access:  read_only
        .address_space:  global
        .offset:         48
        .size:           8
        .value_kind:     global_buffer
      - .offset:         56
        .size:           4
        .value_kind:     hidden_block_count_x
      - .offset:         60
        .size:           4
        .value_kind:     hidden_block_count_y
      - .offset:         64
        .size:           4
        .value_kind:     hidden_block_count_z
      - .offset:         68
        .size:           2
        .value_kind:     hidden_group_size_x
      - .offset:         70
        .size:           2
        .value_kind:     hidden_group_size_y
      - .offset:         72
        .size:           2
        .value_kind:     hidden_group_size_z
      - .offset:         74
        .size:           2
        .value_kind:     hidden_remainder_x
      - .offset:         76
        .size:           2
        .value_kind:     hidden_remainder_y
      - .offset:         78
        .size:           2
        .value_kind:     hidden_remainder_z
      - .offset:         96
        .size:           8
        .value_kind:     hidden_global_offset_x
      - .offset:         104
        .size:           8
        .value_kind:     hidden_global_offset_y
      - .offset:         112
        .size:           8
        .value_kind:     hidden_global_offset_z
      - .offset:         120
        .size:           2
        .value_kind:     hidden_grid_dims
      - .offset:         176
        .size:           4
        .value_kind:     hidden_dynamic_lds_size
    .group_segment_fixed_size: 0
    .kernarg_segment_align: 8
    .kernarg_segment_size: 312
    .language:       OpenCL C
    .language_version:
      - 2
      - 0
    .max_flat_workgroup_size: 512
    .name:           _Z5gemm8ILi128ELi2ELi2ELi2ELi1ELi16EEvPKDF16_S1_iiiPDF16_PfPKf
    .private_segment_fixed_size: 0
    .sgpr_count:     30
    .sgpr_spill_count: 0
    .symbol:         _Z5gemm8ILi128ELi2ELi2ELi2ELi1ELi16EEvPKDF16_S1_iiiPDF16_PfPKf.kd
    .uniform_work_group_size: 1
    .uses_dynamic_stack: false
    .vgpr_count:     90
    .vgpr_spill_count: 0
    .wavefront_size: 64
  - .agpr_count:     0
    .args:
      - .address_space:  global
        .offset:         0
        .size:           8
        .value_kind:     global_buffer
      - .address_space:  global
        .offset:         8
        .size:           8
        .value_kind:     global_buffer
      - .offset:         16
        .size:           4
        .value_kind:     by_value
      - .offset:         20
        .size:           4
        .value_kind:     by_value
      - .offset:         24
        .size:           4
        .value_kind:     by_value
      - .actual_access:  read_only
        .address_space:  global
        .offset:         32
        .size:           8
        .value_kind:     global_buffer
      - .address_space:  global
        .offset:         40
        .size:           8
        .value_kind:     global_buffer
      - .actual_access:  read_only
        .address_space:  global
        .offset:         48
        .size:           8
        .value_kind:     global_buffer
      - .offset:         56
        .size:           4
        .value_kind:     hidden_block_count_x
      - .offset:         60
        .size:           4
        .value_kind:     hidden_block_count_y
      - .offset:         64
        .size:           4
        .value_kind:     hidden_block_count_z
      - .offset:         68
        .size:           2
        .value_kind:     hidden_group_size_x
      - .offset:         70
        .size:           2
        .value_kind:     hidden_group_size_y
      - .offset:         72
        .size:           2
        .value_kind:     hidden_group_size_z
      - .offset:         74
        .size:           2
        .value_kind:     hidden_remainder_x
      - .offset:         76
        .size:           2
        .value_kind:     hidden_remainder_y
      - .offset:         78
        .size:           2
        .value_kind:     hidden_remainder_z
      - .offset:         96
        .size:           8
        .value_kind:     hidden_global_offset_x
      - .offset:         104
        .size:           8
        .value_kind:     hidden_global_offset_y
      - .offset:         112
        .size:           8
        .value_kind:     hidden_global_offset_z
      - .offset:         120
        .size:           2
        .value_kind:     hidden_grid_dims
      - .offset:         176
        .size:           4
        .value_kind:     hidden_dynamic_lds_size
    .group_segment_fixed_size: 0
    .kernarg_segment_align: 8
    .kernarg_segment_size: 312
    .language:       OpenCL C
    .language_version:
      - 2
      - 0
    .max_flat_workgroup_size: 512
    .name:           _Z5gemm8ILi64ELi4ELi6ELi1ELi1ELi16EEvPKDF16_S1_iiiPDF16_PfPKf
    .private_segment_fixed_size: 0
    .sgpr_count:     34
    .sgpr_spill_count: 0
    .symbol:         _Z5gemm8ILi64ELi4ELi6ELi1ELi1ELi16EEvPKDF16_S1_iiiPDF16_PfPKf.kd
    .uniform_work_group_size: 1
    .uses_dynamic_stack: false
    .vgpr_count:     104
    .vgpr_spill_count: 0
    .wavefront_size: 64
  - .agpr_count:     0
    .args:
      - .address_space:  global
        .offset:         0
        .size:           8
        .value_kind:     global_buffer
      - .address_space:  global
        .offset:         8
        .size:           8
        .value_kind:     global_buffer
      - .offset:         16
        .size:           4
        .value_kind:     by_value
      - .offset:         20
        .size:           4
        .value_kind:     by_value
      - .offset:         24
        .size:           4
        .value_kind:     by_value
      - .actual_access:  write_only
        .address_space:  global
        .offset:         32
        .size:           8
        .value_kind:     global_buffer
      - .actual_access:  read_only
        .address_space:  global
        .offset:         40
        .size:           8
        .value_kind:     global_buffer
      - .actual_access:  read_only
        .address_space:  global
        .offset:         48
        .size:           8
        .value_kind:     global_buffer
    .group_segment_fixed_size: 0
    .kernarg_segment_align: 8
    .kernarg_segment_size: 56
    .language:       OpenCL C
    .language_version:
      - 2
      - 0
    .max_flat_workgroup_size: 512
    .name:           _Z5gemm8ILi128ELi2ELi4ELi4ELi2ELi32EEvPKDF16_S1_iiiPDF16_PfPKf
    .private_segment_fixed_size: 0
    .sgpr_count:     38
    .sgpr_spill_count: 0
    .symbol:         _Z5gemm8ILi128ELi2ELi4ELi4ELi2ELi32EEvPKDF16_S1_iiiPDF16_PfPKf.kd
    .uniform_work_group_size: 1
    .uses_dynamic_stack: false
    .vgpr_count:     107
    .vgpr_spill_count: 0
    .wavefront_size: 64
  - .agpr_count:     0
    .args:
      - .actual_access:  read_only
        .address_space:  global
        .offset:         0
        .size:           8
        .value_kind:     global_buffer
      - .actual_access:  read_only
        .address_space:  global
        .offset:         8
        .size:           8
        .value_kind:     global_buffer
      - .actual_access:  read_only
        .address_space:  global
        .offset:         16
        .size:           8
        .value_kind:     global_buffer
      - .address_space:  global
        .offset:         24
        .size:           8
        .value_kind:     global_buffer
      - .actual_access:  read_only
        .address_space:  global
        .offset:         32
        .size:           8
        .value_kind:     global_buffer
      - .actual_access:  read_only
        .address_space:  global
        .offset:         40
        .size:           8
        .value_kind:     global_buffer
      - .actual_access:  write_only
        .address_space:  global
        .offset:         48
        .size:           8
        .value_kind:     global_buffer
    .group_segment_fixed_size: 0
    .kernarg_segment_align: 8
    .kernarg_segment_size: 56
    .language:       OpenCL C
    .language_version:
      - 2
      - 0
    .max_flat_workgroup_size: 256
    .name:           _Z9ln_kernelILi2EEvPKiPKfS3_PfS3_S3_PDF16_
    .private_segment_fixed_size: 0
    .sgpr_count:     18
    .sgpr_spill_count: 0
    .symbol:         _Z9ln_kernelILi2EEvPKiPKfS3_PfS3_S3_PDF16_.kd
    .uniform_work_group_size: 1
    .uses_dynamic_stack: false
    .vgpr_count:     88
    .vgpr_spill_count: 0
    .wavefront_size: 64
  - .agpr_count:     0
    .args:
      - .actual_access:  read_only
        .address_space:  global
        .offset:         0
        .size:           8
        .value_kind:     global_buffer
      - .actual_access:  read_only
        .address_space:  global
        .offset:         8
        .size:           8
        .value_kind:     global_buffer
      - .actual_access:  read_only
        .address_space:  global
        .offset:         16
        .size:           8
        .value_kind:     global_buffer
      - .actual_access:  read_only
        .address_space:  global
        .offset:         24
        .size:           8
        .value_kind:     global_buffer
      - .actual_access:  read_only
        .address_space:  global
        .offset:         32
        .size:           8
        .value_kind:     global_buffer
      - .actual_access:  read_only
        .address_space:  global
        .offset:         40
        .size:           8
        .value_kind:     global_buffer
      - .actual_access:  write_only
        .address_space:  global
        .offset:         48
        .size:           8
        .value_kind:     global_buffer
    .group_segment_fixed_size: 0
    .kernarg_segment_align: 8
    .kernarg_segment_size: 56
    .language:       OpenCL C
    .language_version:
      - 2
      - 0
    .max_flat_workgroup_size: 256
    .name:           _Z9ln_kernelILi0EEvPKiPKfS3_PfS3_S3_PDF16_
    .private_segment_fixed_size: 0
    .sgpr_count:     18
    .sgpr_spill_count: 0
    .symbol:         _Z9ln_kernelILi0EEvPKiPKfS3_PfS3_S3_PDF16_.kd
    .uniform_work_group_size: 1
    .uses_dynamic_stack: false
    .vgpr_count:     60
    .vgpr_spill_count: 0
    .wavefront_size: 64
  - .agpr_count:     0
    .args:
      - .actual_access:  read_only
        .address_space:  global
        .offset:         0
        .size:           8
        .value_kind:     global_buffer
      - .actual_access:  read_only
        .address_space:  global
        .offset:         8
        .size:           8
        .value_kind:     global_buffer
      - .actual_access:  read_only
        .address_space:  global
        .offset:         16
        .size:           8
        .value_kind:     global_buffer
      - .actual_access:  read_only
        .address_space:  global
        .offset:         24
        .size:           8
        .value_kind:     global_buffer
      - .actual_access:  read_only
        .address_space:  global
        .offset:         32
        .size:           8
        .value_kind:     global_buffer
      - .actual_access:  read_only
        .address_space:  global
        .offset:         40
        .size:           8
        .value_kind:     global_buffer
      - .actual_access:  write_only
        .address_space:  global
        .offset:         48
        .size:           8
        .value_kind:     global_buffer
    .group_segment_fixed_size: 0
    .kernarg_segment_align: 8
    .kernarg_segment_size: 56
    .language:       OpenCL C
    .language_version:
      - 2
      - 0
    .max_flat_workgroup_size: 256
    .name:           _Z9ln_kernelILi4EEvPKiPKfS3_PfS3_S3_PDF16_
    .private_segment_fixed_size: 0
    .sgpr_count:     18
    .sgpr_spill_count: 0
    .symbol:         _Z9ln_kernelILi4EEvPKiPKfS3_PfS3_S3_PDF16_.kd
    .uniform_work_group_size: 1
    .uses_dynamic_stack: false
    .vgpr_count:     64
    .vgpr_spill_count: 0
    .wavefront_size: 64
